# diff_mfma: waves 4-7 run PV of previous tile first (half-tile stagger, 3-stage V ring)
# speedup vs baseline: 1.0040x; 1.0040x over previous
.LBB0_1006:
	s_lshl_b32 s4, s8, 7
	v_readlane_b32 s6, v253, 4
	s_or_b32 s4, s4, s6
	v_readlane_b32 s6, v253, 5
	v_or_b32_e32 v0, s4, v224
	v_readlane_b32 s7, v253, 6
	s_movk_i32 s9, 0x1a00
	s_waitcnt lgkmcnt(0)
	v_lshl_add_u64 v[206:207], s[6:7], 0, v[0:1]
	v_mad_u64_u32 v[2:3], s[6:7], v206, s9, v[198:199]
	v_mad_i32_i24 v3, v207, s9, v3
	s_barrier
	global_load_dwordx4 v[114:117], v[2:3], off offset:3584
	global_load_dwordx4 v[118:121], v[2:3], off offset:3616
	global_load_dwordx4 v[122:125], v[2:3], off offset:3648
	global_load_dwordx4 v[126:129], v[2:3], off offset:3680
	global_load_dwordx4 v[130:133], v[188:189], off
	global_load_dwordx4 v[134:137], v[190:191], off
	global_load_dwordx4 v[138:141], v[192:193], off
	global_load_dwordx4 v[142:145], v[194:195], off
	s_movk_i32 s50, 0x1a00
	s_mov_b32 s10, 1
	s_lshl_b32 s18, s8, 1
	s_lshr_b32 s11, s4, 6
	v_readlane_b32 s6, v255, 7
	s_waitcnt vmcnt(3)
	ds_write_b128 v244, v[130:133]
	s_waitcnt vmcnt(1)
	ds_write_b128 v244, v[138:141] offset:8704
	ds_write_b128 v201, v[134:137] offset:17408
	s_waitcnt vmcnt(0)
	ds_write_b128 v201, v[142:145] offset:27648
	v_mov_b32_e32 v0, s6
	s_waitcnt lgkmcnt(0)
	s_barrier
	ds_read_b32 v66, v0
	v_mov_b32_e32 v14, v1
	v_mov_b32_e32 v15, v1
	v_mov_b32_e32 v0, v1
	v_mov_b32_e32 v2, v1
	v_mov_b32_e32 v3, v1
	v_mov_b32_e32 v4, v1
	v_mov_b32_e32 v5, v1
	v_mov_b32_e32 v6, v1
	v_mov_b32_e32 v7, v1
	v_mov_b32_e32 v8, v1
	v_mov_b32_e32 v9, v1
	v_mov_b32_e32 v10, v1
	v_mov_b32_e32 v11, v1
	v_mov_b32_e32 v12, v1
	v_mov_b32_e32 v13, v1
	v_mov_b64_e32 v[64:65], v[14:15]
	v_mov_b64_e32 v[48:49], v[14:15]
	v_mov_b64_e32 v[32:33], v[14:15]
	s_lshl_b32 s19, s8, 9
	v_mov_b64_e32 v[62:63], v[12:13]
	v_mov_b64_e32 v[60:61], v[10:11]
	v_mov_b64_e32 v[58:59], v[8:9]
	v_mov_b64_e32 v[56:57], v[6:7]
	v_mov_b64_e32 v[54:55], v[4:5]
	v_mov_b64_e32 v[52:53], v[2:3]
	v_mov_b64_e32 v[50:51], v[0:1]
	v_mov_b64_e32 v[46:47], v[12:13]
	v_mov_b64_e32 v[44:45], v[10:11]
	v_mov_b64_e32 v[42:43], v[8:9]
	v_mov_b64_e32 v[40:41], v[6:7]
	v_mov_b64_e32 v[38:39], v[4:5]
	v_mov_b64_e32 v[36:37], v[2:3]
	v_mov_b64_e32 v[34:35], v[0:1]
	v_mov_b64_e32 v[30:31], v[12:13]
	v_mov_b64_e32 v[28:29], v[10:11]
	v_mov_b64_e32 v[26:27], v[8:9]
	v_mov_b64_e32 v[24:25], v[6:7]
	v_mov_b64_e32 v[22:23], v[4:5]
	v_mov_b64_e32 v[20:21], v[2:3]
	v_mov_b64_e32 v[18:19], v[0:1]
	v_mov_b64_e32 v[16:17], v[14:15]
	s_waitcnt lgkmcnt(0)
	v_mov_b32_e32 v67, v66
	v_mov_b32_e32 v68, v66
	v_mov_b32_e32 v69, v66
	v_mov_b32_e32 v70, v66
	v_mov_b32_e32 v71, v66
	v_mov_b32_e32 v72, v66
	v_mov_b32_e32 v73, v66
	v_mov_b32_e32 v74, v66
	v_mov_b32_e32 v75, v66
	v_mov_b32_e32 v76, v66
	v_mov_b32_e32 v77, v66
	v_mov_b32_e32 v78, v66
	v_mov_b32_e32 v79, v66
	v_mov_b32_e32 v80, v66
	v_mov_b32_e32 v81, v66
	s_add_i32 s18, s18, 2
	v_subrev_u32_e32 v184, s19, v181
	v_mov_b32_e32 v205, 0
	s_movk_i32 s20, 0xfe00
	s_movk_i32 s21, 0x26e
	v_mov_b64_e32 v[208:209], v[202:203]
	v_mov_b64_e32 v[14:15], v[12:13]
	v_mov_b64_e32 v[12:13], v[10:11]
	v_mov_b64_e32 v[10:11], v[8:9]
	v_mov_b64_e32 v[8:9], v[6:7]
	v_mov_b64_e32 v[6:7], v[4:5]
	v_mov_b64_e32 v[4:5], v[2:3]
	v_mov_b64_e32 v[2:3], v[0:1]
	v_mov_b32_e32 v0, 0
	s_mov_b32 s26, 0
	s_mov_b32 s27, 0x9400
	s_mov_b32 s28, 0xf100
	v_readlane_b32 s29, v253, 8
	s_nop 3
	s_cmp_lg_u32 s29, 0
	s_cbranch_scc1 .Ldfb_top
	s_branch .LBB0_1008
.LBB0_1007:
	s_addk_i32 s20, 0x100
	s_add_i32 s10, s10, 1
	s_add_i32 s21, s21, 64
	s_mov_b64 s[6:7], 0x68000
	s_mov_b32 s29, s26
	s_mov_b32 s26, s27
	s_mov_b32 s27, s28
	s_mov_b32 s28, s29
	s_cmp_eq_u32 s19, s20
	v_lshl_add_u64 v[208:209], v[208:209], 0, s[6:7]
	s_waitcnt lgkmcnt(0)
	s_barrier
	s_cbranch_scc1 .Ldf_join

.LBB0_1022:
	s_nop 8
	v_exp_f32_e32 v154, v98
	v_exp_f32_e32 v155, v99
	v_exp_f32_e32 v159, v100
	v_exp_f32_e32 v161, v101
	v_exp_f32_e32 v99, v102
	v_exp_f32_e32 v98, v103
	v_exp_f32_e32 v101, v104
	v_exp_f32_e32 v100, v105
	v_exp_f32_e32 v147, v90
	v_exp_f32_e32 v149, v106
	v_exp_f32_e32 v146, v91
	v_exp_f32_e32 v148, v107
	v_exp_f32_e32 v107, v92
	v_exp_f32_e32 v151, v108
	v_exp_f32_e32 v106, v93
	v_exp_f32_e32 v150, v109
	v_exp_f32_e32 v93, v94
	v_exp_f32_e32 v109, v110
	v_exp_f32_e32 v92, v95
	v_exp_f32_e32 v108, v111
	v_exp_f32_e32 v95, v96
	v_exp_f32_e32 v111, v112
	v_exp_f32_e32 v94, v97
	v_exp_f32_e32 v110, v113
	v_exp_f32_e32 v82, v82
	v_exp_f32_e32 v158, v84
	v_exp_f32_e32 v160, v85
	v_exp_f32_e32 v85, v86
	v_exp_f32_e32 v84, v87
	v_exp_f32_e32 v83, v83
	v_exp_f32_e32 v87, v88
	v_exp_f32_e32 v86, v89
	v_pk_mov_b32 v[88:89], v[98:99], v[98:99] op_sel:[1,0]
	v_pk_mov_b32 v[90:91], v[100:101], v[100:101] op_sel:[1,0]
	v_pk_add_f32 v[162:163], v[92:93], v[108:109]
	v_pk_add_f32 v[164:165], v[94:95], v[110:111]
	v_cvt_pk_bf16_f32 v88, v88, v89
	v_cvt_pk_bf16_f32 v89, v90, v91
	v_pk_mov_b32 v[90:91], v[146:147], v[146:147] op_sel:[1,0]
	v_pk_mov_b32 v[96:97], v[106:107], v[106:107] op_sel:[1,0]
	v_pk_mov_b32 v[92:93], v[92:93], v[92:93] op_sel:[1,0]
	v_pk_mov_b32 v[94:95], v[94:95], v[94:95] op_sel:[1,0]
	v_cvt_pk_bf16_f32 v90, v90, v91
	v_cvt_pk_bf16_f32 v91, v96, v97
	v_cvt_pk_bf16_f32 v92, v92, v93
	v_cvt_pk_bf16_f32 v93, v94, v95
	v_pk_mov_b32 v[94:95], v[148:149], v[148:149] op_sel:[1,0]
	v_pk_mov_b32 v[96:97], v[150:151], v[150:151] op_sel:[1,0]
	v_add_f32_e32 v156, v82, v154
	v_pk_add_f32 v[102:103], v[84:85], v[98:99]
	v_cvt_pk_bf16_f32 v94, v94, v95
	v_cvt_pk_bf16_f32 v95, v96, v97
	v_pk_mov_b32 v[96:97], v[108:109], v[108:109] op_sel:[1,0]
	v_pk_mov_b32 v[98:99], v[110:111], v[110:111] op_sel:[1,0]
	v_add_f32_e32 v157, v83, v155
	v_cvt_pk_bf16_f32 v96, v96, v97
	v_cvt_pk_bf16_f32 v97, v98, v99
	v_add_f32_e32 v98, 0, v156
	v_add_f32_e32 v166, v158, v159
	v_add_f32_e32 v98, v157, v98
	v_add_f32_e32 v167, v160, v161
	v_add_f32_e32 v98, v166, v98
	v_add_f32_e32 v98, v167, v98
	v_add_f32_e32 v98, v103, v98
	v_pk_add_f32 v[104:105], v[86:87], v[100:101]
	v_add_f32_e32 v98, v102, v98
	v_add_f32_e32 v98, v105, v98
	v_pk_add_f32 v[112:113], v[146:147], v[148:149]
	v_add_f32_e32 v98, v104, v98
	v_add_f32_e32 v98, v113, v98
	v_pk_add_f32 v[152:153], v[106:107], v[150:151]
	v_add_f32_e32 v98, v112, v98
	v_pk_mov_b32 v[84:85], v[84:85], v[84:85] op_sel:[1,0]
	v_pk_mov_b32 v[86:87], v[86:87], v[86:87] op_sel:[1,0]
	v_add_f32_e32 v98, v153, v98
	v_add3_u32 v167, s26, v240, v241
	v_cvt_pk_bf16_f32 v82, v82, v83
	v_cvt_pk_bf16_f32 v83, v158, v160
	v_cvt_pk_bf16_f32 v84, v84, v85
	v_cvt_pk_bf16_f32 v85, v86, v87
	v_cvt_pk_bf16_f32 v86, v154, v155
	v_cvt_pk_bf16_f32 v87, v159, v161
	v_add_f32_e32 v166, v152, v98
	ds_read_b64_tr_b16 v[98:99], v167 offset:17408
	ds_read_b64_tr_b16 v[100:101], v167 offset:19968
	ds_read_b64_tr_b16 v[104:105], v167 offset:20032
	ds_read_b64_tr_b16 v[102:103], v167 offset:17472
	ds_read_b64_tr_b16 v[106:107], v167 offset:22528
	ds_read_b64_tr_b16 v[108:109], v167 offset:25088
	ds_read_b64_tr_b16 v[112:113], v167 offset:25152
	ds_read_b64_tr_b16 v[110:111], v167 offset:22592
	ds_read_b64_tr_b16 v[146:147], v167 offset:27648
	ds_read_b64_tr_b16 v[148:149], v167 offset:30208
	ds_read_b64_tr_b16 v[152:153], v167 offset:30272
	ds_read_b64_tr_b16 v[150:151], v167 offset:27712
	ds_read_b64_tr_b16 v[154:155], v167 offset:32768
	ds_read_b64_tr_b16 v[156:157], v167 offset:35328
	ds_read_b64_tr_b16 v[160:161], v167 offset:35392
	ds_read_b64_tr_b16 v[158:159], v167 offset:32832
	v_add_f32_e32 v163, v163, v166
	v_add_f32_e32 v162, v162, v163
	v_add_f32_e32 v162, v165, v162
	v_add_f32_e32 v162, v164, v162
	s_waitcnt lgkmcnt(14)
	v_mfma_f32_32x32x16_bf16 v[50:65], v[98:101], v[82:85], v[50:65]
	s_waitcnt lgkmcnt(10)
	v_mfma_f32_32x32x16_bf16 v[50:65], v[106:109], v[90:93], v[50:65]
	s_waitcnt lgkmcnt(6)
	v_mfma_f32_32x32x16_bf16 v[50:65], v[146:149], v[86:89], v[50:65]
	s_waitcnt lgkmcnt(2)
	v_mfma_f32_32x32x16_bf16 v[50:65], v[154:157], v[94:97], v[50:65]
	ds_read_b64_tr_b16 v[98:99], v167 offset:22656
	ds_read_b64_tr_b16 v[100:101], v167 offset:25216
	ds_read_b64_tr_b16 v[106:107], v167 offset:27776
	ds_read_b64_tr_b16 v[108:109], v167 offset:30336
	ds_read_b64_tr_b16 v[146:147], v167 offset:17536
	ds_read_b64_tr_b16 v[148:149], v167 offset:20096
	ds_read_b64_tr_b16 v[154:155], v167 offset:32896
	ds_read_b64_tr_b16 v[156:157], v167 offset:35456
	v_mfma_f32_32x32x16_bf16 v[34:49], v[102:105], v[82:85], v[34:49]
	v_mfma_f32_32x32x16_bf16 v[34:49], v[110:113], v[90:93], v[34:49]
	v_mfma_f32_32x32x16_bf16 v[34:49], v[150:153], v[86:89], v[34:49]
	s_waitcnt lgkmcnt(8)
	v_mfma_f32_32x32x16_bf16 v[34:49], v[158:161], v[94:97], v[34:49]
	ds_read_b64_tr_b16 v[102:103], v167 offset:22720
	ds_read_b64_tr_b16 v[104:105], v167 offset:25280
	ds_read_b64_tr_b16 v[110:111], v167 offset:27840
	ds_read_b64_tr_b16 v[112:113], v167 offset:30400
	ds_read_b64_tr_b16 v[150:151], v167 offset:17600
	ds_read_b64_tr_b16 v[152:153], v167 offset:20160
	ds_read_b64_tr_b16 v[158:159], v167 offset:32960
	ds_read_b64_tr_b16 v[160:161], v167 offset:35520
	s_waitcnt lgkmcnt(10)
	v_mfma_f32_32x32x16_bf16 v[18:33], v[146:149], v[82:85], v[18:33]
	v_mfma_f32_32x32x16_bf16 v[18:33], v[98:101], v[90:93], v[18:33]
	v_mfma_f32_32x32x16_bf16 v[18:33], v[106:109], v[86:89], v[18:33]
	s_waitcnt lgkmcnt(8)
	v_mfma_f32_32x32x16_bf16 v[18:33], v[154:157], v[94:97], v[18:33]
	s_waitcnt lgkmcnt(2)
	v_mfma_f32_32x32x16_bf16 v[2:17], v[150:153], v[82:85], v[2:17]
	v_add_f32_e32 v205, v205, v162
	v_mfma_f32_32x32x16_bf16 v[2:17], v[102:105], v[90:93], v[2:17]
	v_mfma_f32_32x32x16_bf16 v[2:17], v[110:113], v[86:89], v[2:17]
	s_waitcnt lgkmcnt(0)
	v_mfma_f32_32x32x16_bf16 v[2:17], v[158:161], v[94:97], v[2:17]
	s_andn2_b64 vcc, exec, s[6:7]
	s_cbranch_vccnz .LBB0_1007
.LBB0_1023:
	s_bitcmp1_b32 s10, 0
	s_cselect_b32 s6, 0x9400, 0
	s_add_i32 s6, s6, 0
	v_add_u32_e32 v82, s6, v182
	v_add_u32_e32 v83, s27, v200
	s_waitcnt vmcnt(3)
	ds_write_b128 v82, v[130:133]
	s_waitcnt vmcnt(1)
	ds_write_b128 v82, v[138:141] offset:8704
	ds_write_b128 v83, v[134:137] offset:17408
	s_waitcnt vmcnt(0)
	ds_write_b128 v83, v[142:145] offset:27648
	s_branch .LBB0_1007

.Ldfb_top:
	s_cmp_lt_u32 s10, s18
	s_cselect_b64 s[6:7], -1, 0
	s_cbranch_scc0 .Ldfb_nopf
	v_add_co_u32_e32 v218, vcc, 0xfffcc000, v208
	s_nop 1
	v_addc_co_u32_e32 v219, vcc, -1, v209, vcc
	global_load_dwordx4 v[130:133], v[218:219], off offset:-1024
	global_load_dwordx4 v[134:137], v[218:219], off
	global_load_dwordx4 v[138:141], v[208:209], off offset:-1024
	global_load_dwordx4 v[142:145], v[208:209], off
.Ldfb_nopf:
	s_cmp_eq_u32 s10, 1
	s_cbranch_scc1 .Ldfb_nopv
	v_add3_u32 v167, s28, v240, v241
	ds_read_b64_tr_b16 v[98:99], v167 offset:17408
	ds_read_b64_tr_b16 v[100:101], v167 offset:19968
	ds_read_b64_tr_b16 v[104:105], v167 offset:20032
	ds_read_b64_tr_b16 v[102:103], v167 offset:17472
	ds_read_b64_tr_b16 v[106:107], v167 offset:22528
	ds_read_b64_tr_b16 v[108:109], v167 offset:25088
	ds_read_b64_tr_b16 v[112:113], v167 offset:25152
	ds_read_b64_tr_b16 v[110:111], v167 offset:22592
	ds_read_b64_tr_b16 v[146:147], v167 offset:27648
	ds_read_b64_tr_b16 v[148:149], v167 offset:30208
	ds_read_b64_tr_b16 v[152:153], v167 offset:30272
	ds_read_b64_tr_b16 v[150:151], v167 offset:27712
	ds_read_b64_tr_b16 v[154:155], v167 offset:32768
	ds_read_b64_tr_b16 v[156:157], v167 offset:35328
	ds_read_b64_tr_b16 v[160:161], v167 offset:35392
	ds_read_b64_tr_b16 v[158:159], v167 offset:32832
	s_waitcnt lgkmcnt(14)
	v_mfma_f32_32x32x16_bf16 v[50:65], v[98:101], v[82:85], v[50:65]
	s_waitcnt lgkmcnt(10)
	v_mfma_f32_32x32x16_bf16 v[50:65], v[106:109], v[90:93], v[50:65]
	s_waitcnt lgkmcnt(6)
	v_mfma_f32_32x32x16_bf16 v[50:65], v[146:149], v[86:89], v[50:65]
	s_waitcnt lgkmcnt(2)
	v_mfma_f32_32x32x16_bf16 v[50:65], v[154:157], v[94:97], v[50:65]
	ds_read_b64_tr_b16 v[98:99], v167 offset:22656
	ds_read_b64_tr_b16 v[100:101], v167 offset:25216
	ds_read_b64_tr_b16 v[106:107], v167 offset:27776
	ds_read_b64_tr_b16 v[108:109], v167 offset:30336
	ds_read_b64_tr_b16 v[146:147], v167 offset:17536
	ds_read_b64_tr_b16 v[148:149], v167 offset:20096
	ds_read_b64_tr_b16 v[154:155], v167 offset:32896
	ds_read_b64_tr_b16 v[156:157], v167 offset:35456
	v_mfma_f32_32x32x16_bf16 v[34:49], v[102:105], v[82:85], v[34:49]
	v_mfma_f32_32x32x16_bf16 v[34:49], v[110:113], v[90:93], v[34:49]
	v_mfma_f32_32x32x16_bf16 v[34:49], v[150:153], v[86:89], v[34:49]
	s_waitcnt lgkmcnt(8)
	v_mfma_f32_32x32x16_bf16 v[34:49], v[158:161], v[94:97], v[34:49]
	ds_read_b64_tr_b16 v[102:103], v167 offset:22720
	ds_read_b64_tr_b16 v[104:105], v167 offset:25280
	ds_read_b64_tr_b16 v[110:111], v167 offset:27840
	ds_read_b64_tr_b16 v[112:113], v167 offset:30400
	ds_read_b64_tr_b16 v[150:151], v167 offset:17600
	ds_read_b64_tr_b16 v[152:153], v167 offset:20160
	ds_read_b64_tr_b16 v[158:159], v167 offset:32960
	ds_read_b64_tr_b16 v[160:161], v167 offset:35520
	s_waitcnt lgkmcnt(10)
	v_mfma_f32_32x32x16_bf16 v[18:33], v[146:149], v[82:85], v[18:33]
	v_mfma_f32_32x32x16_bf16 v[18:33], v[98:101], v[90:93], v[18:33]
	v_mfma_f32_32x32x16_bf16 v[18:33], v[106:109], v[86:89], v[18:33]
	s_waitcnt lgkmcnt(8)
	v_mfma_f32_32x32x16_bf16 v[18:33], v[154:157], v[94:97], v[18:33]
	s_waitcnt lgkmcnt(2)
	v_mfma_f32_32x32x16_bf16 v[2:17], v[150:153], v[82:85], v[2:17]
	v_mfma_f32_32x32x16_bf16 v[2:17], v[102:105], v[90:93], v[2:17]
	v_mfma_f32_32x32x16_bf16 v[2:17], v[110:113], v[86:89], v[2:17]
	s_waitcnt lgkmcnt(0)
	v_mfma_f32_32x32x16_bf16 v[2:17], v[158:161], v[94:97], v[2:17]
.Ldfb_nopv:
	s_add_i32 s8, s10, -1
	s_cmp_gt_u32 s8, s11
	s_cbranch_scc1 .Ldfb_skipc
	s_bitcmp1_b32 s8, 0
	s_cselect_b32 s8, 0x9400, 0
	s_add_i32 s22, s8, 0
	v_add3_u32 v82, s22, v225, v239
	ds_read_b128 v[170:173], v82
	ds_read_b128 v[166:169], v82 offset:32
	ds_read_b128 v[174:177], v82 offset:8704
	ds_read_b128 v[158:161], v82 offset:8736
	ds_read_b128 v[154:157], v82 offset:64
	ds_read_b128 v[146:149], v82 offset:96
	ds_read_b128 v[162:165], v82 offset:8768
	ds_read_b128 v[150:153], v82 offset:8800
	s_cmp_le_u32 s21, s4
	s_mov_b64 s[8:9], -1
	s_cbranch_scc0 .Ldfb_1014
	s_waitcnt lgkmcnt(7)
	v_mfma_f32_32x32x16_bf16 v[82:97], v[170:173], v[114:117], v[66:81]
	s_mov_b64 s[8:9], 0
	s_waitcnt lgkmcnt(5)
	v_mfma_f32_32x32x16_bf16 v[98:113], v[174:177], v[114:117], v[66:81]

.Ldfb_1022:
	s_nop 8
	v_exp_f32_e32 v154, v98
	v_exp_f32_e32 v155, v99
	v_exp_f32_e32 v159, v100
	v_exp_f32_e32 v161, v101
	v_exp_f32_e32 v99, v102
	v_exp_f32_e32 v98, v103
	v_exp_f32_e32 v101, v104
	v_exp_f32_e32 v100, v105
	v_exp_f32_e32 v147, v90
	v_exp_f32_e32 v149, v106
	v_exp_f32_e32 v146, v91
	v_exp_f32_e32 v148, v107
	v_exp_f32_e32 v107, v92
	v_exp_f32_e32 v151, v108
	v_exp_f32_e32 v106, v93
	v_exp_f32_e32 v150, v109
	v_exp_f32_e32 v93, v94
	v_exp_f32_e32 v109, v110
	v_exp_f32_e32 v92, v95
	v_exp_f32_e32 v108, v111
	v_exp_f32_e32 v95, v96
	v_exp_f32_e32 v111, v112
	v_exp_f32_e32 v94, v97
	v_exp_f32_e32 v110, v113
	v_exp_f32_e32 v82, v82
	v_exp_f32_e32 v158, v84
	v_exp_f32_e32 v160, v85
	v_exp_f32_e32 v85, v86
	v_exp_f32_e32 v84, v87
	v_exp_f32_e32 v83, v83
	v_exp_f32_e32 v87, v88
	v_exp_f32_e32 v86, v89
	v_pk_mov_b32 v[88:89], v[98:99], v[98:99] op_sel:[1,0]
	v_pk_mov_b32 v[90:91], v[100:101], v[100:101] op_sel:[1,0]
	v_pk_add_f32 v[162:163], v[92:93], v[108:109]
	v_pk_add_f32 v[164:165], v[94:95], v[110:111]
	v_cvt_pk_bf16_f32 v88, v88, v89
	v_cvt_pk_bf16_f32 v89, v90, v91
	v_pk_mov_b32 v[90:91], v[146:147], v[146:147] op_sel:[1,0]
	v_pk_mov_b32 v[96:97], v[106:107], v[106:107] op_sel:[1,0]
	v_pk_mov_b32 v[92:93], v[92:93], v[92:93] op_sel:[1,0]
	v_pk_mov_b32 v[94:95], v[94:95], v[94:95] op_sel:[1,0]
	v_cvt_pk_bf16_f32 v90, v90, v91
	v_cvt_pk_bf16_f32 v91, v96, v97
	v_cvt_pk_bf16_f32 v92, v92, v93
	v_cvt_pk_bf16_f32 v93, v94, v95
	v_pk_mov_b32 v[94:95], v[148:149], v[148:149] op_sel:[1,0]
	v_pk_mov_b32 v[96:97], v[150:151], v[150:151] op_sel:[1,0]
	v_add_f32_e32 v156, v82, v154
	v_pk_add_f32 v[102:103], v[84:85], v[98:99]
	v_cvt_pk_bf16_f32 v94, v94, v95
	v_cvt_pk_bf16_f32 v95, v96, v97
	v_pk_mov_b32 v[96:97], v[108:109], v[108:109] op_sel:[1,0]
	v_pk_mov_b32 v[98:99], v[110:111], v[110:111] op_sel:[1,0]
	v_add_f32_e32 v157, v83, v155
	v_cvt_pk_bf16_f32 v96, v96, v97
	v_cvt_pk_bf16_f32 v97, v98, v99
	v_add_f32_e32 v98, 0, v156
	v_add_f32_e32 v166, v158, v159
	v_add_f32_e32 v98, v157, v98
	v_add_f32_e32 v167, v160, v161
	v_add_f32_e32 v98, v166, v98
	v_add_f32_e32 v98, v167, v98
	v_add_f32_e32 v98, v103, v98
	v_pk_add_f32 v[104:105], v[86:87], v[100:101]
	v_add_f32_e32 v98, v102, v98
	v_add_f32_e32 v98, v105, v98
	v_pk_add_f32 v[112:113], v[146:147], v[148:149]
	v_add_f32_e32 v98, v104, v98
	v_add_f32_e32 v98, v113, v98
	v_pk_add_f32 v[152:153], v[106:107], v[150:151]
	v_add_f32_e32 v98, v112, v98
	v_pk_mov_b32 v[84:85], v[84:85], v[84:85] op_sel:[1,0]
	v_pk_mov_b32 v[86:87], v[86:87], v[86:87] op_sel:[1,0]
	v_add_f32_e32 v98, v153, v98
	v_cvt_pk_bf16_f32 v82, v82, v83
	v_cvt_pk_bf16_f32 v83, v158, v160
	v_cvt_pk_bf16_f32 v84, v84, v85
	v_cvt_pk_bf16_f32 v85, v86, v87
	v_cvt_pk_bf16_f32 v86, v154, v155
	v_cvt_pk_bf16_f32 v87, v159, v161
	v_add_f32_e32 v166, v152, v98
	v_add_f32_e32 v163, v163, v166
	v_add_f32_e32 v162, v162, v163
	v_add_f32_e32 v162, v165, v162
	v_add_f32_e32 v162, v164, v162
	v_add_f32_e32 v205, v205, v162
.Ldfb_skipc:
	s_andn2_b64 vcc, exec, s[6:7]
	s_cbranch_vccnz .Ldfb_end
	s_bitcmp1_b32 s10, 0
	s_cselect_b32 s6, 0x9400, 0
	v_add_u32_e32 v218, s6, v182
	v_add_u32_e32 v219, s27, v200
	s_waitcnt vmcnt(3)
	ds_write_b128 v218, v[130:133]
	s_waitcnt vmcnt(1)
	ds_write_b128 v218, v[138:141] offset:8704
	ds_write_b128 v219, v[134:137] offset:17408
	s_waitcnt vmcnt(0)
	ds_write_b128 v219, v[142:145] offset:27648
	s_branch .Ldfb_end
.Ldfb_tail:
	s_add_i32 s8, s10, -2
	s_cmp_gt_u32 s8, s11
	s_cbranch_scc1 .Ldf_join
	v_add3_u32 v167, s28, v240, v241
	ds_read_b64_tr_b16 v[98:99], v167 offset:17408
	ds_read_b64_tr_b16 v[100:101], v167 offset:19968
	ds_read_b64_tr_b16 v[104:105], v167 offset:20032
	ds_read_b64_tr_b16 v[102:103], v167 offset:17472
	ds_read_b64_tr_b16 v[106:107], v167 offset:22528
	ds_read_b64_tr_b16 v[108:109], v167 offset:25088
	ds_read_b64_tr_b16 v[112:113], v167 offset:25152
	ds_read_b64_tr_b16 v[110:111], v167 offset:22592
	ds_read_b64_tr_b16 v[146:147], v167 offset:27648
	ds_read_b64_tr_b16 v[148:149], v167 offset:30208
	ds_read_b64_tr_b16 v[152:153], v167 offset:30272
	ds_read_b64_tr_b16 v[150:151], v167 offset:27712
	ds_read_b64_tr_b16 v[154:155], v167 offset:32768
	ds_read_b64_tr_b16 v[156:157], v167 offset:35328
	ds_read_b64_tr_b16 v[160:161], v167 offset:35392
	ds_read_b64_tr_b16 v[158:159], v167 offset:32832
	s_waitcnt lgkmcnt(14)
	v_mfma_f32_32x32x16_bf16 v[50:65], v[98:101], v[82:85], v[50:65]
	s_waitcnt lgkmcnt(10)
	v_mfma_f32_32x32x16_bf16 v[50:65], v[106:109], v[90:93], v[50:65]
	s_waitcnt lgkmcnt(6)
	v_mfma_f32_32x32x16_bf16 v[50:65], v[146:149], v[86:89], v[50:65]
	s_waitcnt lgkmcnt(2)
	v_mfma_f32_32x32x16_bf16 v[50:65], v[154:157], v[94:97], v[50:65]
	ds_read_b64_tr_b16 v[98:99], v167 offset:22656
	ds_read_b64_tr_b16 v[100:101], v167 offset:25216
	ds_read_b64_tr_b16 v[106:107], v167 offset:27776
	ds_read_b64_tr_b16 v[108:109], v167 offset:30336
	ds_read_b64_tr_b16 v[146:147], v167 offset:17536
	ds_read_b64_tr_b16 v[148:149], v167 offset:20096
	ds_read_b64_tr_b16 v[154:155], v167 offset:32896
	ds_read_b64_tr_b16 v[156:157], v167 offset:35456
	v_mfma_f32_32x32x16_bf16 v[34:49], v[102:105], v[82:85], v[34:49]
	v_mfma_f32_32x32x16_bf16 v[34:49], v[110:113], v[90:93], v[34:49]
	v_mfma_f32_32x32x16_bf16 v[34:49], v[150:153], v[86:89], v[34:49]
	s_waitcnt lgkmcnt(8)
	v_mfma_f32_32x32x16_bf16 v[34:49], v[158:161], v[94:97], v[34:49]
	ds_read_b64_tr_b16 v[102:103], v167 offset:22720
	ds_read_b64_tr_b16 v[104:105], v167 offset:25280
	ds_read_b64_tr_b16 v[110:111], v167 offset:27840
	ds_read_b64_tr_b16 v[112:113], v167 offset:30400
	ds_read_b64_tr_b16 v[150:151], v167 offset:17600
	ds_read_b64_tr_b16 v[152:153], v167 offset:20160
	ds_read_b64_tr_b16 v[158:159], v167 offset:32960
	ds_read_b64_tr_b16 v[160:161], v167 offset:35520
	s_waitcnt lgkmcnt(10)
	v_mfma_f32_32x32x16_bf16 v[18:33], v[146:149], v[82:85], v[18:33]
	v_mfma_f32_32x32x16_bf16 v[18:33], v[98:101], v[90:93], v[18:33]
	v_mfma_f32_32x32x16_bf16 v[18:33], v[106:109], v[86:89], v[18:33]
	s_waitcnt lgkmcnt(8)
	v_mfma_f32_32x32x16_bf16 v[18:33], v[154:157], v[94:97], v[18:33]
	s_waitcnt lgkmcnt(2)
	v_mfma_f32_32x32x16_bf16 v[2:17], v[150:153], v[82:85], v[2:17]
	v_mfma_f32_32x32x16_bf16 v[2:17], v[102:105], v[90:93], v[2:17]
	v_mfma_f32_32x32x16_bf16 v[2:17], v[110:113], v[86:89], v[2:17]
	s_waitcnt lgkmcnt(0)
	v_mfma_f32_32x32x16_bf16 v[2:17], v[158:161], v[94:97], v[2:17]
.Ldf_join:
	s_barrier
